# lean3 attention loop with the in-loop barrier 5 fragments early
# baseline (speedup 1.0000x reference)
.Lattn_pa0:
	s_waitcnt lgkmcnt(6)
	v_mfma_f32_16x16x32_bf16 v[64:67], v[160:163], v[96:99], 0
	v_exp_f32_e32 v88, v88
	v_mfma_f32_16x16x32_bf16 v[68:71], v[160:163], v[112:115], 0
	v_exp_f32_e32 v92, v92
	ds_read_b128 v[160:163], v201 offset:20480
	s_add_u32 s15, s22, s12
	s_addc_u32 s14, s23, s13
	s_add_u32 s6, s15, 0x23a50000
	s_addc_u32 s7, s14, 0
	v_mfma_f32_16x16x32_bf16 v[0:3], v[164:167], v[216:219], v[0:3]
	v_cvt_pk_bf16_f32 v242, v80, v81
	v_mfma_f32_16x16x32_bf16 v[4:7], v[164:167], v[238:241], v[4:7]
	v_exp_f32_e32 v89, v89
	ds_read_b128 v[164:167], v209 offset:8192
	s_waitcnt vmcnt(4)
	ds_write_b128 v225, v[152:155] offset:49152
	s_waitcnt lgkmcnt(7)
	v_mfma_f32_16x16x32_bf16 v[68:71], v[168:171], v[116:119], v[68:71]
	v_exp_f32_e32 v93, v93
	v_mfma_f32_16x16x32_bf16 v[64:67], v[168:171], v[100:103], v[64:67]
	v_cvt_pk_bf16_f32 v243, v82, v83
	ds_read_b128 v[168:171], v202 offset:20480
	v_mfma_f32_16x16x32_bf16 v[12:15], v[172:175], v[238:241], v[12:15]
	v_exp_f32_e32 v90, v90
	v_mfma_f32_16x16x32_bf16 v[8:11], v[172:175], v[216:219], v[8:11]
	v_exp_f32_e32 v94, v94
	ds_read_b128 v[172:175], v209 offset:10240
	s_waitcnt lgkmcnt(7)
	v_mfma_f32_16x16x32_bf16 v[64:67], v[176:179], v[104:107], v[64:67]
	v_cvt_pk_bf16_f32 v204, v84, v85
	v_mfma_f32_16x16x32_bf16 v[68:71], v[176:179], v[120:123], v[68:71]
	v_exp_f32_e32 v91, v91
	ds_read_b128 v[176:179], v203 offset:20480
	ds_write_b128 v226, v[156:159] offset:49152
	v_mfma_f32_16x16x32_bf16 v[16:19], v[180:183], v[216:219], v[16:19]
	v_exp_f32_e32 v95, v95
	v_mfma_f32_16x16x32_bf16 v[20:23], v[180:183], v[238:241], v[20:23]
	v_cvt_pk_bf16_f32 v205, v86, v87
	v_add_f32_e32 v220, v220, v88
	ds_read_b128 v[180:183], v209 offset:12288
	s_waitcnt lgkmcnt(8)
	v_mfma_f32_16x16x32_bf16 v[68:71], v[230:233], v[124:127], v[68:71]
	v_add_f32_e32 v221, v221, v92
	v_add_f32_e32 v220, v220, v89
	v_mfma_f32_16x16x32_bf16 v[64:67], v[230:233], v[108:111], v[64:67]
	v_add_f32_e32 v221, v221, v93
	v_cvt_pk_bf16_f32 v244, v88, v89
	ds_read_b128 v[230:233], v246 offset:20480
	v_mfma_f32_16x16x32_bf16 v[28:31], v[234:237], v[238:241], v[28:31]
	v_cvt_pk_bf16_f32 v245, v90, v91
	v_cvt_pk_bf16_f32 v206, v92, v93
	v_mfma_f32_16x16x32_bf16 v[24:27], v[234:237], v[216:219], v[24:27]
	v_cvt_pk_bf16_f32 v207, v94, v95
	ds_read_b128 v[234:237], v209 offset:14336
	ds_write_b64 v227, v[132:133] offset:32768
	s_waitcnt lgkmcnt(9)
	v_mfma_f32_16x16x32_bf16 v[72:75], v[160:163], v[96:99], 0
	v_add_f32_e32 v220, v220, v90
	v_add_f32_e32 v221, v221, v94
	v_mfma_f32_16x16x32_bf16 v[76:79], v[160:163], v[112:115], 0
	v_add_f32_e32 v220, v220, v91
	v_add_f32_e32 v221, v221, v95
	ds_read_b128 v[160:163], v201 offset:24576
	v_mfma_f32_16x16x32_bf16 v[32:35], v[164:167], v[216:219], v[32:35]
	v_add_f32_e32 v194, v194, v220
	v_add_f32_e32 v195, v195, v221
	v_mfma_f32_16x16x32_bf16 v[36:39], v[164:167], v[238:241], v[36:39]
	v_exp_f32_e32 v64, v64
	ds_read_b128 v[164:167], v210 offset:0
	s_waitcnt lgkmcnt(8)
	v_mfma_f32_16x16x32_bf16 v[76:79], v[168:171], v[116:119], v[76:79]
	v_exp_f32_e32 v68, v68
	v_mfma_f32_16x16x32_bf16 v[72:75], v[168:171], v[100:103], v[72:75]
	v_exp_f32_e32 v65, v65
	ds_read_b128 v[168:171], v202 offset:24576
	ds_write_b64 v228, v[134:135] offset:32768
	v_mfma_f32_16x16x32_bf16 v[44:47], v[172:175], v[238:241], v[44:47]
	v_exp_f32_e32 v69, v69
	v_mfma_f32_16x16x32_bf16 v[40:43], v[172:175], v[216:219], v[40:43]
	v_exp_f32_e32 v66, v66
	ds_read_b128 v[172:175], v210 offset:2048
	s_waitcnt lgkmcnt(8)
	v_mfma_f32_16x16x32_bf16 v[72:75], v[176:179], v[104:107], v[72:75]
	v_exp_f32_e32 v70, v70
	v_mfma_f32_16x16x32_bf16 v[76:79], v[176:179], v[120:123], v[76:79]
	v_exp_f32_e32 v67, v67
	ds_read_b128 v[176:179], v203 offset:24576
	v_mfma_f32_16x16x32_bf16 v[48:51], v[180:183], v[216:219], v[48:51]
	v_exp_f32_e32 v71, v71
	v_mfma_f32_16x16x32_bf16 v[52:55], v[180:183], v[238:241], v[52:55]
	v_add_f32_e32 v220, v64, v65
	ds_read_b128 v[180:183], v210 offset:4096
	ds_write_b64 v229, v[128:129] offset:32768
	s_waitcnt lgkmcnt(9)
	v_mfma_f32_16x16x32_bf16 v[76:79], v[230:233], v[124:127], v[76:79]
	v_add_f32_e32 v221, v68, v69
	v_mfma_f32_16x16x32_bf16 v[72:75], v[230:233], v[108:111], v[72:75]
	v_add_f32_e32 v220, v220, v66
	ds_read_b128 v[230:233], v246 offset:24576
	v_mfma_f32_16x16x32_bf16 v[60:63], v[234:237], v[238:241], v[60:63]
	v_add_f32_e32 v221, v221, v70
	v_add_f32_e32 v220, v220, v67
	v_mfma_f32_16x16x32_bf16 v[56:59], v[234:237], v[216:219], v[56:59]
	v_add_f32_e32 v221, v221, v71
	ds_read_b128 v[234:237], v210 offset:6144
	s_waitcnt lgkmcnt(8)
	v_mfma_f32_16x16x32_bf16 v[80:83], v[160:163], v[96:99], 0
	v_exp_f32_e32 v72, v72
	v_mfma_f32_16x16x32_bf16 v[84:87], v[160:163], v[112:115], 0
	v_exp_f32_e32 v76, v76
	ds_read_b128 v[160:163], v201 offset:28672
	ds_write_b64 v184, v[130:131] offset:32768
	v_mfma_f32_16x16x32_bf16 v[0:3], v[164:167], v[242:245], v[0:3]
	v_exp_f32_e32 v73, v73
	v_mfma_f32_16x16x32_bf16 v[4:7], v[164:167], v[204:207], v[4:7]
	v_exp_f32_e32 v77, v77
	ds_read_b128 v[164:167], v210 offset:8192
	s_waitcnt lgkmcnt(8)
	v_mfma_f32_16x16x32_bf16 v[84:87], v[168:171], v[116:119], v[84:87]
	v_exp_f32_e32 v74, v74
	v_mfma_f32_16x16x32_bf16 v[80:83], v[168:171], v[100:103], v[80:83]
	v_exp_f32_e32 v78, v78
	ds_read_b128 v[168:171], v202 offset:28672
	v_mfma_f32_16x16x32_bf16 v[12:15], v[172:175], v[204:207], v[12:15]
	v_exp_f32_e32 v75, v75
	v_mfma_f32_16x16x32_bf16 v[8:11], v[172:175], v[242:245], v[8:11]
	v_exp_f32_e32 v79, v79
	ds_read_b128 v[172:175], v210 offset:10240
	global_load_dwordx4 v[132:135], v198, s[8:9]
	s_waitcnt lgkmcnt(8)
	v_mfma_f32_16x16x32_bf16 v[80:83], v[176:179], v[104:107], v[80:83]
	v_add_f32_e32 v220, v220, v72
	v_add_f32_e32 v221, v221, v76
	v_mfma_f32_16x16x32_bf16 v[84:87], v[176:179], v[120:123], v[84:87]
	v_add_f32_e32 v220, v220, v73
	ds_read_b128 v[176:179], v203 offset:28672
	v_mfma_f32_16x16x32_bf16 v[16:19], v[180:183], v[242:245], v[16:19]
	v_add_f32_e32 v221, v221, v77
	v_add_f32_e32 v220, v220, v74
	v_mfma_f32_16x16x32_bf16 v[20:23], v[180:183], v[204:207], v[20:23]
	v_add_f32_e32 v221, v221, v78
	ds_read_b128 v[180:183], v210 offset:12288
	s_waitcnt lgkmcnt(7)
	v_mfma_f32_16x16x32_bf16 v[84:87], v[230:233], v[124:127], v[84:87]
	v_add_f32_e32 v220, v220, v75
	v_add_f32_e32 v221, v221, v79
	v_mfma_f32_16x16x32_bf16 v[80:83], v[230:233], v[108:111], v[80:83]
	v_cvt_pk_bf16_f32 v216, v64, v65
	ds_read_b128 v[230:233], v246 offset:28672
	global_load_dwordx4 v[128:131], v199, s[8:9]
	v_mfma_f32_16x16x32_bf16 v[28:31], v[234:237], v[204:207], v[28:31]
	v_cvt_pk_bf16_f32 v217, v66, v67
	v_cvt_pk_bf16_f32 v238, v68, v69
	v_mfma_f32_16x16x32_bf16 v[24:27], v[234:237], v[242:245], v[24:27]
	v_cvt_pk_bf16_f32 v239, v70, v71
	ds_read_b128 v[234:237], v210 offset:14336
	s_waitcnt lgkmcnt(6)
	v_mfma_f32_16x16x32_bf16 v[88:91], v[160:163], v[96:99], 0
	v_exp_f32_e32 v80, v80
	v_mfma_f32_16x16x32_bf16 v[92:95], v[160:163], v[112:115], 0
	v_exp_f32_e32 v84, v84
	ds_read_b128 v[160:163], v201 offset:32768
	v_mfma_f32_16x16x32_bf16 v[32:35], v[164:167], v[242:245], v[32:35]
	v_exp_f32_e32 v81, v81
	v_mfma_f32_16x16x32_bf16 v[36:39], v[164:167], v[204:207], v[36:39]
	v_exp_f32_e32 v85, v85
	ds_read_b128 v[164:167], v209 offset:16384
	global_load_dwordx4 v[152:155], v196, s[6:7]
	s_waitcnt lgkmcnt(6)
	v_mfma_f32_16x16x32_bf16 v[92:95], v[168:171], v[116:119], v[92:95]
	v_exp_f32_e32 v82, v82
	v_mfma_f32_16x16x32_bf16 v[88:91], v[168:171], v[100:103], v[88:91]
	v_exp_f32_e32 v86, v86
	ds_read_b128 v[168:171], v202 offset:32768
	v_mfma_f32_16x16x32_bf16 v[44:47], v[172:175], v[204:207], v[44:47]
	v_exp_f32_e32 v83, v83
	v_mfma_f32_16x16x32_bf16 v[40:43], v[172:175], v[242:245], v[40:43]
	v_exp_f32_e32 v87, v87
	ds_read_b128 v[172:175], v209 offset:18432
	s_waitcnt lgkmcnt(6)
	v_mfma_f32_16x16x32_bf16 v[88:91], v[176:179], v[104:107], v[88:91]
	v_add_f32_e32 v220, v220, v80
	v_add_f32_e32 v221, v221, v84
	v_mfma_f32_16x16x32_bf16 v[92:95], v[176:179], v[120:123], v[92:95]
	v_add_f32_e32 v220, v220, v81
	ds_read_b128 v[176:179], v203 offset:32768
	global_load_dwordx4 v[156:159], v197, s[6:7]
	v_mfma_f32_16x16x32_bf16 v[48:51], v[180:183], v[242:245], v[48:51]
	v_add_f32_e32 v221, v221, v85
	v_add_f32_e32 v220, v220, v82
	v_mfma_f32_16x16x32_bf16 v[52:55], v[180:183], v[204:207], v[52:55]
	v_add_f32_e32 v221, v221, v86
	ds_read_b128 v[180:183], v209 offset:20480
	s_waitcnt lgkmcnt(6)
	v_mfma_f32_16x16x32_bf16 v[92:95], v[230:233], v[124:127], v[92:95]
	v_add_f32_e32 v220, v220, v83
	v_add_f32_e32 v221, v221, v87
	v_mfma_f32_16x16x32_bf16 v[88:91], v[230:233], v[108:111], v[88:91]
	v_cvt_pk_bf16_f32 v218, v72, v73
	ds_read_b128 v[230:233], v246 offset:32768
	v_mfma_f32_16x16x32_bf16 v[60:63], v[234:237], v[204:207], v[60:63]
	v_cvt_pk_bf16_f32 v219, v74, v75
	v_cvt_pk_bf16_f32 v240, v76, v77
	v_mfma_f32_16x16x32_bf16 v[56:59], v[234:237], v[242:245], v[56:59]
	v_cvt_pk_bf16_f32 v241, v78, v79
	ds_read_b128 v[234:237], v209 offset:22528
	s_setprio 0
	s_waitcnt lgkmcnt(6)
	v_mfma_f32_16x16x32_bf16 v[64:67], v[160:163], v[96:99], 0
	v_exp_f32_e32 v88, v88
	v_mfma_f32_16x16x32_bf16 v[68:71], v[160:163], v[112:115], 0
	v_exp_f32_e32 v92, v92
	ds_read_b128 v[160:163], v201 offset:36864
	s_add_u32 s6, s15, 0x23a60000
	s_addc_u32 s7, s14, 0
	v_mfma_f32_16x16x32_bf16 v[0:3], v[164:167], v[216:219], v[0:3]
	v_cvt_pk_bf16_f32 v242, v80, v81
	v_mfma_f32_16x16x32_bf16 v[4:7], v[164:167], v[238:241], v[4:7]
	v_exp_f32_e32 v89, v89
	ds_read_b128 v[164:167], v209 offset:24576
	s_waitcnt vmcnt(4)
	ds_write_b128 v225, v[136:139] offset:0
	s_waitcnt lgkmcnt(7)
	v_mfma_f32_16x16x32_bf16 v[68:71], v[168:171], v[116:119], v[68:71]
	v_exp_f32_e32 v93, v93
	v_mfma_f32_16x16x32_bf16 v[64:67], v[168:171], v[100:103], v[64:67]
	v_cvt_pk_bf16_f32 v243, v82, v83
	ds_read_b128 v[168:171], v202 offset:36864
	v_mfma_f32_16x16x32_bf16 v[12:15], v[172:175], v[238:241], v[12:15]
	v_exp_f32_e32 v90, v90
	v_mfma_f32_16x16x32_bf16 v[8:11], v[172:175], v[216:219], v[8:11]
	v_exp_f32_e32 v94, v94
	ds_read_b128 v[172:175], v209 offset:26624
	s_waitcnt lgkmcnt(7)
	v_mfma_f32_16x16x32_bf16 v[64:67], v[176:179], v[104:107], v[64:67]
	v_cvt_pk_bf16_f32 v204, v84, v85
	v_mfma_f32_16x16x32_bf16 v[68:71], v[176:179], v[120:123], v[68:71]
	v_exp_f32_e32 v91, v91
	ds_read_b128 v[176:179], v203 offset:36864
	ds_write_b128 v226, v[140:143] offset:0
	v_mfma_f32_16x16x32_bf16 v[16:19], v[180:183], v[216:219], v[16:19]
	v_exp_f32_e32 v95, v95
	v_mfma_f32_16x16x32_bf16 v[20:23], v[180:183], v[238:241], v[20:23]
	v_cvt_pk_bf16_f32 v205, v86, v87
	v_add_f32_e32 v220, v220, v88
	ds_read_b128 v[180:183], v209 offset:28672
	s_waitcnt lgkmcnt(8)
	v_mfma_f32_16x16x32_bf16 v[68:71], v[230:233], v[124:127], v[68:71]
	v_add_f32_e32 v221, v221, v92
	v_add_f32_e32 v220, v220, v89
	v_mfma_f32_16x16x32_bf16 v[64:67], v[230:233], v[108:111], v[64:67]
	v_add_f32_e32 v221, v221, v93
	v_cvt_pk_bf16_f32 v244, v88, v89
	ds_read_b128 v[230:233], v246 offset:36864
	v_mfma_f32_16x16x32_bf16 v[28:31], v[234:237], v[238:241], v[28:31]
	v_cvt_pk_bf16_f32 v245, v90, v91
	v_cvt_pk_bf16_f32 v206, v92, v93
	v_mfma_f32_16x16x32_bf16 v[24:27], v[234:237], v[216:219], v[24:27]
	v_cvt_pk_bf16_f32 v207, v94, v95
	ds_read_b128 v[234:237], v209 offset:30720
	ds_write_b64 v227, v[148:149] offset:49152
	s_waitcnt lgkmcnt(9)
	v_mfma_f32_16x16x32_bf16 v[72:75], v[160:163], v[96:99], 0
	v_add_f32_e32 v220, v220, v90
	v_add_f32_e32 v221, v221, v94
	v_mfma_f32_16x16x32_bf16 v[76:79], v[160:163], v[112:115], 0
	v_add_f32_e32 v220, v220, v91
	v_add_f32_e32 v221, v221, v95
	ds_read_b128 v[160:163], v201 offset:40960
	v_mfma_f32_16x16x32_bf16 v[32:35], v[164:167], v[216:219], v[32:35]
	v_add_f32_e32 v194, v194, v220
	v_add_f32_e32 v195, v195, v221
	v_mfma_f32_16x16x32_bf16 v[36:39], v[164:167], v[238:241], v[36:39]
	v_exp_f32_e32 v64, v64
	ds_read_b128 v[164:167], v210 offset:16384
	s_waitcnt lgkmcnt(8)
	v_mfma_f32_16x16x32_bf16 v[76:79], v[168:171], v[116:119], v[76:79]
	v_exp_f32_e32 v68, v68
	v_mfma_f32_16x16x32_bf16 v[72:75], v[168:171], v[100:103], v[72:75]
	v_exp_f32_e32 v65, v65
	ds_read_b128 v[168:171], v202 offset:40960
	ds_write_b64 v228, v[150:151] offset:49152
	v_mfma_f32_16x16x32_bf16 v[44:47], v[172:175], v[238:241], v[44:47]
	v_exp_f32_e32 v69, v69
	v_mfma_f32_16x16x32_bf16 v[40:43], v[172:175], v[216:219], v[40:43]
	v_exp_f32_e32 v66, v66
	ds_read_b128 v[172:175], v210 offset:18432
	s_waitcnt lgkmcnt(8)
	v_mfma_f32_16x16x32_bf16 v[72:75], v[176:179], v[104:107], v[72:75]
	v_exp_f32_e32 v70, v70
	v_mfma_f32_16x16x32_bf16 v[76:79], v[176:179], v[120:123], v[76:79]
	v_exp_f32_e32 v67, v67
	ds_read_b128 v[176:179], v203 offset:40960
	v_mfma_f32_16x16x32_bf16 v[48:51], v[180:183], v[216:219], v[48:51]
	v_exp_f32_e32 v71, v71
	v_mfma_f32_16x16x32_bf16 v[52:55], v[180:183], v[238:241], v[52:55]
	v_add_f32_e32 v220, v64, v65
	ds_read_b128 v[180:183], v210 offset:20480
	ds_write_b64 v229, v[144:145] offset:49152
	s_waitcnt lgkmcnt(9)
	v_mfma_f32_16x16x32_bf16 v[76:79], v[230:233], v[124:127], v[76:79]
	v_add_f32_e32 v221, v68, v69
	v_mfma_f32_16x16x32_bf16 v[72:75], v[230:233], v[108:111], v[72:75]
	v_add_f32_e32 v220, v220, v66
	ds_read_b128 v[230:233], v246 offset:40960
	v_mfma_f32_16x16x32_bf16 v[60:63], v[234:237], v[238:241], v[60:63]
	v_add_f32_e32 v221, v221, v70
	v_add_f32_e32 v220, v220, v67
	v_mfma_f32_16x16x32_bf16 v[56:59], v[234:237], v[216:219], v[56:59]
	v_add_f32_e32 v221, v221, v71
	ds_read_b128 v[234:237], v210 offset:22528
	s_waitcnt lgkmcnt(8)
	v_mfma_f32_16x16x32_bf16 v[80:83], v[160:163], v[96:99], 0
	v_exp_f32_e32 v72, v72
	v_mfma_f32_16x16x32_bf16 v[84:87], v[160:163], v[112:115], 0
	v_exp_f32_e32 v76, v76
	ds_read_b128 v[160:163], v201 offset:45056
	ds_write_b64 v184, v[146:147] offset:49152
	v_mfma_f32_16x16x32_bf16 v[0:3], v[164:167], v[242:245], v[0:3]
	v_exp_f32_e32 v73, v73
	v_mfma_f32_16x16x32_bf16 v[4:7], v[164:167], v[204:207], v[4:7]
	v_exp_f32_e32 v77, v77
	ds_read_b128 v[164:167], v210 offset:24576
	s_waitcnt lgkmcnt(8)
	v_mfma_f32_16x16x32_bf16 v[84:87], v[168:171], v[116:119], v[84:87]
	v_exp_f32_e32 v74, v74
	v_mfma_f32_16x16x32_bf16 v[80:83], v[168:171], v[100:103], v[80:83]
	v_exp_f32_e32 v78, v78
	ds_read_b128 v[168:171], v202 offset:45056
	v_mfma_f32_16x16x32_bf16 v[12:15], v[172:175], v[204:207], v[12:15]
	v_exp_f32_e32 v75, v75
	v_mfma_f32_16x16x32_bf16 v[8:11], v[172:175], v[242:245], v[8:11]
	v_exp_f32_e32 v79, v79
	ds_read_b128 v[172:175], v210 offset:26624
	global_load_dwordx4 v[148:151], v198, s[8:9] offset:128
	s_waitcnt lgkmcnt(8)
	v_mfma_f32_16x16x32_bf16 v[80:83], v[176:179], v[104:107], v[80:83]
	v_add_f32_e32 v220, v220, v72
	v_add_f32_e32 v221, v221, v76
	v_mfma_f32_16x16x32_bf16 v[84:87], v[176:179], v[120:123], v[84:87]
	v_add_f32_e32 v220, v220, v73
	ds_read_b128 v[176:179], v203 offset:45056
	v_mfma_f32_16x16x32_bf16 v[16:19], v[180:183], v[242:245], v[16:19]
	v_add_f32_e32 v221, v221, v77
	v_add_f32_e32 v220, v220, v74
	v_mfma_f32_16x16x32_bf16 v[20:23], v[180:183], v[204:207], v[20:23]
	v_add_f32_e32 v221, v221, v78
	ds_read_b128 v[180:183], v210 offset:28672
	s_waitcnt lgkmcnt(7)
	v_mfma_f32_16x16x32_bf16 v[84:87], v[230:233], v[124:127], v[84:87]
	v_add_f32_e32 v220, v220, v75
	v_add_f32_e32 v221, v221, v79
	v_mfma_f32_16x16x32_bf16 v[80:83], v[230:233], v[108:111], v[80:83]
	v_cvt_pk_bf16_f32 v216, v64, v65
	ds_read_b128 v[230:233], v246 offset:45056
	global_load_dwordx4 v[144:147], v199, s[8:9] offset:128
	v_mfma_f32_16x16x32_bf16 v[28:31], v[234:237], v[204:207], v[28:31]
	v_cvt_pk_bf16_f32 v217, v66, v67
	v_cvt_pk_bf16_f32 v238, v68, v69
	v_mfma_f32_16x16x32_bf16 v[24:27], v[234:237], v[242:245], v[24:27]
	v_cvt_pk_bf16_f32 v239, v70, v71
	ds_read_b128 v[234:237], v210 offset:30720
	s_waitcnt lgkmcnt(6)
	v_mfma_f32_16x16x32_bf16 v[88:91], v[160:163], v[96:99], 0
	v_exp_f32_e32 v80, v80
	v_mfma_f32_16x16x32_bf16 v[92:95], v[160:163], v[112:115], 0
	v_exp_f32_e32 v84, v84
	v_mfma_f32_16x16x32_bf16 v[32:35], v[164:167], v[242:245], v[32:35]
	v_exp_f32_e32 v81, v81
	v_mfma_f32_16x16x32_bf16 v[36:39], v[164:167], v[204:207], v[36:39]
	v_exp_f32_e32 v85, v85
	global_load_dwordx4 v[136:139], v196, s[6:7]
	s_waitcnt lgkmcnt(5)
	v_mfma_f32_16x16x32_bf16 v[92:95], v[168:171], v[116:119], v[92:95]
	v_exp_f32_e32 v82, v82
	v_mfma_f32_16x16x32_bf16 v[88:91], v[168:171], v[100:103], v[88:91]
	v_exp_f32_e32 v86, v86
	s_waitcnt lgkmcnt(0)
	s_barrier
	ds_read_b128 v[160:163], v201 offset:49152
	ds_read_b128 v[164:167], v209 offset:32768
	ds_read_b128 v[168:171], v202 offset:49152
	v_mfma_f32_16x16x32_bf16 v[44:47], v[172:175], v[204:207], v[44:47]
	v_exp_f32_e32 v83, v83
	v_mfma_f32_16x16x32_bf16 v[40:43], v[172:175], v[242:245], v[40:43]
	v_exp_f32_e32 v87, v87
	ds_read_b128 v[172:175], v209 offset:34816
	v_mfma_f32_16x16x32_bf16 v[88:91], v[176:179], v[104:107], v[88:91]
	v_add_f32_e32 v220, v220, v80
	v_add_f32_e32 v221, v221, v84
	v_mfma_f32_16x16x32_bf16 v[92:95], v[176:179], v[120:123], v[92:95]
	v_add_f32_e32 v220, v220, v81
	ds_read_b128 v[176:179], v203 offset:49152
	global_load_dwordx4 v[140:143], v197, s[6:7]
	v_mfma_f32_16x16x32_bf16 v[48:51], v[180:183], v[242:245], v[48:51]
	v_add_f32_e32 v221, v221, v85
	v_add_f32_e32 v220, v220, v82
	v_mfma_f32_16x16x32_bf16 v[52:55], v[180:183], v[204:207], v[52:55]
	v_add_f32_e32 v221, v221, v86
	ds_read_b128 v[180:183], v209 offset:36864
	v_mfma_f32_16x16x32_bf16 v[92:95], v[230:233], v[124:127], v[92:95]
	v_add_f32_e32 v220, v220, v83
	v_add_f32_e32 v221, v221, v87
	v_mfma_f32_16x16x32_bf16 v[88:91], v[230:233], v[108:111], v[88:91]
	v_cvt_pk_bf16_f32 v218, v72, v73
	ds_read_b128 v[230:233], v246 offset:49152
	v_mfma_f32_16x16x32_bf16 v[60:63], v[234:237], v[204:207], v[60:63]
	v_cvt_pk_bf16_f32 v219, v74, v75
	v_cvt_pk_bf16_f32 v240, v76, v77
	v_mfma_f32_16x16x32_bf16 v[56:59], v[234:237], v[242:245], v[56:59]
	v_cvt_pk_bf16_f32 v241, v78, v79
	ds_read_b128 v[234:237], v209 offset:38912
	s_cmp_eq_u32 s100, 0
	s_cbranch_scc1 .Lattn_pa2
	s_setprio 1
.Lattn_pa2:
	s_waitcnt lgkmcnt(6)
	v_mfma_f32_16x16x32_bf16 v[64:67], v[160:163], v[96:99], 0
	v_exp_f32_e32 v88, v88
	v_mfma_f32_16x16x32_bf16 v[68:71], v[160:163], v[112:115], 0
	v_exp_f32_e32 v92, v92
	ds_read_b128 v[160:163], v201 offset:53248
	s_add_u32 s6, s15, 0x23a70000
	s_addc_u32 s7, s14, 0
	v_mfma_f32_16x16x32_bf16 v[0:3], v[164:167], v[216:219], v[0:3]
	v_cvt_pk_bf16_f32 v242, v80, v81
	v_mfma_f32_16x16x32_bf16 v[4:7], v[164:167], v[238:241], v[4:7]
	v_exp_f32_e32 v89, v89
	ds_read_b128 v[164:167], v209 offset:40960
	s_waitcnt vmcnt(4)
	ds_write_b128 v225, v[152:155] offset:16384
	s_waitcnt lgkmcnt(7)
	v_mfma_f32_16x16x32_bf16 v[68:71], v[168:171], v[116:119], v[68:71]
	v_exp_f32_e32 v93, v93
	v_mfma_f32_16x16x32_bf16 v[64:67], v[168:171], v[100:103], v[64:67]
	v_cvt_pk_bf16_f32 v243, v82, v83
	ds_read_b128 v[168:171], v202 offset:53248
	v_mfma_f32_16x16x32_bf16 v[12:15], v[172:175], v[238:241], v[12:15]
	v_exp_f32_e32 v90, v90
	v_mfma_f32_16x16x32_bf16 v[8:11], v[172:175], v[216:219], v[8:11]
	v_exp_f32_e32 v94, v94
	ds_read_b128 v[172:175], v209 offset:43008
	s_waitcnt lgkmcnt(7)
	v_mfma_f32_16x16x32_bf16 v[64:67], v[176:179], v[104:107], v[64:67]
	v_cvt_pk_bf16_f32 v204, v84, v85
	v_mfma_f32_16x16x32_bf16 v[68:71], v[176:179], v[120:123], v[68:71]
	v_exp_f32_e32 v91, v91
	ds_read_b128 v[176:179], v203 offset:53248
	ds_write_b128 v226, v[156:159] offset:16384
	v_mfma_f32_16x16x32_bf16 v[16:19], v[180:183], v[216:219], v[16:19]
	v_exp_f32_e32 v95, v95
	v_mfma_f32_16x16x32_bf16 v[20:23], v[180:183], v[238:241], v[20:23]
	v_cvt_pk_bf16_f32 v205, v86, v87
	v_add_f32_e32 v220, v220, v88
	ds_read_b128 v[180:183], v209 offset:45056
	s_waitcnt lgkmcnt(8)
	v_mfma_f32_16x16x32_bf16 v[68:71], v[230:233], v[124:127], v[68:71]
	v_add_f32_e32 v221, v221, v92
	v_add_f32_e32 v220, v220, v89
	v_mfma_f32_16x16x32_bf16 v[64:67], v[230:233], v[108:111], v[64:67]
	v_add_f32_e32 v221, v221, v93
	v_cvt_pk_bf16_f32 v244, v88, v89
	ds_read_b128 v[230:233], v246 offset:53248
	v_mfma_f32_16x16x32_bf16 v[28:31], v[234:237], v[238:241], v[28:31]
	v_cvt_pk_bf16_f32 v245, v90, v91
	v_cvt_pk_bf16_f32 v206, v92, v93
	v_mfma_f32_16x16x32_bf16 v[24:27], v[234:237], v[216:219], v[24:27]
	v_cvt_pk_bf16_f32 v207, v94, v95
	ds_read_b128 v[234:237], v209 offset:47104
	ds_write_b64 v227, v[132:133] offset:0
	s_waitcnt lgkmcnt(9)
	v_mfma_f32_16x16x32_bf16 v[72:75], v[160:163], v[96:99], 0
	v_add_f32_e32 v220, v220, v90
	v_add_f32_e32 v221, v221, v94
	v_mfma_f32_16x16x32_bf16 v[76:79], v[160:163], v[112:115], 0
	v_add_f32_e32 v220, v220, v91
	v_add_f32_e32 v221, v221, v95
	ds_read_b128 v[160:163], v201 offset:57344
	v_mfma_f32_16x16x32_bf16 v[32:35], v[164:167], v[216:219], v[32:35]
	v_add_f32_e32 v194, v194, v220
	v_add_f32_e32 v195, v195, v221
	v_mfma_f32_16x16x32_bf16 v[36:39], v[164:167], v[238:241], v[36:39]
	v_exp_f32_e32 v64, v64
	ds_read_b128 v[164:167], v210 offset:32768
	s_waitcnt lgkmcnt(8)
	v_mfma_f32_16x16x32_bf16 v[76:79], v[168:171], v[116:119], v[76:79]
	v_exp_f32_e32 v68, v68
	v_mfma_f32_16x16x32_bf16 v[72:75], v[168:171], v[100:103], v[72:75]
	v_exp_f32_e32 v65, v65
	ds_read_b128 v[168:171], v202 offset:57344
	ds_write_b64 v228, v[134:135] offset:0
	v_mfma_f32_16x16x32_bf16 v[44:47], v[172:175], v[238:241], v[44:47]
	v_exp_f32_e32 v69, v69
	v_mfma_f32_16x16x32_bf16 v[40:43], v[172:175], v[216:219], v[40:43]
	v_exp_f32_e32 v66, v66
	ds_read_b128 v[172:175], v210 offset:34816
	s_waitcnt lgkmcnt(8)
	v_mfma_f32_16x16x32_bf16 v[72:75], v[176:179], v[104:107], v[72:75]
	v_exp_f32_e32 v70, v70
	v_mfma_f32_16x16x32_bf16 v[76:79], v[176:179], v[120:123], v[76:79]
	v_exp_f32_e32 v67, v67
	ds_read_b128 v[176:179], v203 offset:57344
	v_mfma_f32_16x16x32_bf16 v[48:51], v[180:183], v[216:219], v[48:51]
	v_exp_f32_e32 v71, v71
	v_mfma_f32_16x16x32_bf16 v[52:55], v[180:183], v[238:241], v[52:55]
	v_add_f32_e32 v220, v64, v65
	ds_read_b128 v[180:183], v210 offset:36864
	ds_write_b64 v229, v[128:129] offset:0
	s_waitcnt lgkmcnt(9)
	v_mfma_f32_16x16x32_bf16 v[76:79], v[230:233], v[124:127], v[76:79]
	v_add_f32_e32 v221, v68, v69
	v_mfma_f32_16x16x32_bf16 v[72:75], v[230:233], v[108:111], v[72:75]
	v_add_f32_e32 v220, v220, v66
	ds_read_b128 v[230:233], v246 offset:57344
	v_mfma_f32_16x16x32_bf16 v[60:63], v[234:237], v[238:241], v[60:63]
	v_add_f32_e32 v221, v221, v70
	v_add_f32_e32 v220, v220, v67
	v_mfma_f32_16x16x32_bf16 v[56:59], v[234:237], v[216:219], v[56:59]
	v_add_f32_e32 v221, v221, v71
	ds_read_b128 v[234:237], v210 offset:38912
	s_waitcnt lgkmcnt(8)
	v_mfma_f32_16x16x32_bf16 v[80:83], v[160:163], v[96:99], 0
	v_exp_f32_e32 v72, v72
	v_mfma_f32_16x16x32_bf16 v[84:87], v[160:163], v[112:115], 0
	v_exp_f32_e32 v76, v76
	ds_read_b128 v[160:163], v201 offset:61440
	ds_write_b64 v184, v[130:131] offset:0
	v_mfma_f32_16x16x32_bf16 v[0:3], v[164:167], v[242:245], v[0:3]
	v_exp_f32_e32 v73, v73
	v_mfma_f32_16x16x32_bf16 v[4:7], v[164:167], v[204:207], v[4:7]
	v_exp_f32_e32 v77, v77
	ds_read_b128 v[164:167], v210 offset:40960
	s_waitcnt lgkmcnt(8)
	v_mfma_f32_16x16x32_bf16 v[84:87], v[168:171], v[116:119], v[84:87]
	v_exp_f32_e32 v74, v74
	v_mfma_f32_16x16x32_bf16 v[80:83], v[168:171], v[100:103], v[80:83]
	v_exp_f32_e32 v78, v78
	ds_read_b128 v[168:171], v202 offset:61440
	v_mfma_f32_16x16x32_bf16 v[12:15], v[172:175], v[204:207], v[12:15]
	v_exp_f32_e32 v75, v75
	v_mfma_f32_16x16x32_bf16 v[8:11], v[172:175], v[242:245], v[8:11]
	v_exp_f32_e32 v79, v79
	ds_read_b128 v[172:175], v210 offset:43008
	global_load_dwordx4 v[132:135], v198, s[8:9] offset:256
	s_waitcnt lgkmcnt(8)
	v_mfma_f32_16x16x32_bf16 v[80:83], v[176:179], v[104:107], v[80:83]
	v_add_f32_e32 v220, v220, v72
	v_add_f32_e32 v221, v221, v76
	v_mfma_f32_16x16x32_bf16 v[84:87], v[176:179], v[120:123], v[84:87]
	v_add_f32_e32 v220, v220, v73
	ds_read_b128 v[176:179], v203 offset:61440
	v_mfma_f32_16x16x32_bf16 v[16:19], v[180:183], v[242:245], v[16:19]
	v_add_f32_e32 v221, v221, v77
	v_add_f32_e32 v220, v220, v74
	v_mfma_f32_16x16x32_bf16 v[20:23], v[180:183], v[204:207], v[20:23]
	v_add_f32_e32 v221, v221, v78
	ds_read_b128 v[180:183], v210 offset:45056
	s_waitcnt lgkmcnt(7)
	v_mfma_f32_16x16x32_bf16 v[84:87], v[230:233], v[124:127], v[84:87]
	v_add_f32_e32 v220, v220, v75
	v_add_f32_e32 v221, v221, v79
	v_mfma_f32_16x16x32_bf16 v[80:83], v[230:233], v[108:111], v[80:83]
	v_cvt_pk_bf16_f32 v216, v64, v65
	ds_read_b128 v[230:233], v246 offset:61440
	global_load_dwordx4 v[128:131], v199, s[8:9] offset:256
	v_mfma_f32_16x16x32_bf16 v[28:31], v[234:237], v[204:207], v[28:31]
	v_cvt_pk_bf16_f32 v217, v66, v67
	v_cvt_pk_bf16_f32 v238, v68, v69
	v_mfma_f32_16x16x32_bf16 v[24:27], v[234:237], v[242:245], v[24:27]
	v_cvt_pk_bf16_f32 v239, v70, v71
	ds_read_b128 v[234:237], v210 offset:47104
	s_waitcnt lgkmcnt(6)
	v_mfma_f32_16x16x32_bf16 v[88:91], v[160:163], v[96:99], 0
	v_exp_f32_e32 v80, v80
	v_mfma_f32_16x16x32_bf16 v[92:95], v[160:163], v[112:115], 0
	v_exp_f32_e32 v84, v84
	ds_read_b128 v[160:163], v201 offset:0
	v_mfma_f32_16x16x32_bf16 v[32:35], v[164:167], v[242:245], v[32:35]
	v_exp_f32_e32 v81, v81
	v_mfma_f32_16x16x32_bf16 v[36:39], v[164:167], v[204:207], v[36:39]
	v_exp_f32_e32 v85, v85
	ds_read_b128 v[164:167], v209 offset:49152
	global_load_dwordx4 v[152:155], v196, s[6:7]
	s_waitcnt lgkmcnt(6)
	v_mfma_f32_16x16x32_bf16 v[92:95], v[168:171], v[116:119], v[92:95]
	v_exp_f32_e32 v82, v82
	v_mfma_f32_16x16x32_bf16 v[88:91], v[168:171], v[100:103], v[88:91]
	v_exp_f32_e32 v86, v86
	ds_read_b128 v[168:171], v202 offset:0
	v_mfma_f32_16x16x32_bf16 v[44:47], v[172:175], v[204:207], v[44:47]
	v_exp_f32_e32 v83, v83
	v_mfma_f32_16x16x32_bf16 v[40:43], v[172:175], v[242:245], v[40:43]
	v_exp_f32_e32 v87, v87
	ds_read_b128 v[172:175], v209 offset:51200
	s_waitcnt lgkmcnt(6)
	v_mfma_f32_16x16x32_bf16 v[88:91], v[176:179], v[104:107], v[88:91]
	v_add_f32_e32 v220, v220, v80
	v_add_f32_e32 v221, v221, v84
	v_mfma_f32_16x16x32_bf16 v[92:95], v[176:179], v[120:123], v[92:95]
	v_add_f32_e32 v220, v220, v81
	ds_read_b128 v[176:179], v203 offset:0
	global_load_dwordx4 v[156:159], v197, s[6:7]
	v_mfma_f32_16x16x32_bf16 v[48:51], v[180:183], v[242:245], v[48:51]
	v_add_f32_e32 v221, v221, v85
	v_add_f32_e32 v220, v220, v82
	v_mfma_f32_16x16x32_bf16 v[52:55], v[180:183], v[204:207], v[52:55]
	v_add_f32_e32 v221, v221, v86
	ds_read_b128 v[180:183], v209 offset:53248
	s_waitcnt lgkmcnt(6)
	v_mfma_f32_16x16x32_bf16 v[92:95], v[230:233], v[124:127], v[92:95]
	v_add_f32_e32 v220, v220, v83
	v_add_f32_e32 v221, v221, v87
	v_mfma_f32_16x16x32_bf16 v[88:91], v[230:233], v[108:111], v[88:91]
	v_cvt_pk_bf16_f32 v218, v72, v73
	ds_read_b128 v[230:233], v246 offset:0
	v_mfma_f32_16x16x32_bf16 v[60:63], v[234:237], v[204:207], v[60:63]
	v_cvt_pk_bf16_f32 v219, v74, v75
	v_cvt_pk_bf16_f32 v240, v76, v77
	v_mfma_f32_16x16x32_bf16 v[56:59], v[234:237], v[242:245], v[56:59]
	v_cvt_pk_bf16_f32 v241, v78, v79
	ds_read_b128 v[234:237], v209 offset:55296
	s_setprio 0
	s_waitcnt lgkmcnt(6)
	v_mfma_f32_16x16x32_bf16 v[64:67], v[160:163], v[96:99], 0
	v_exp_f32_e32 v88, v88
	v_mfma_f32_16x16x32_bf16 v[68:71], v[160:163], v[112:115], 0
	v_exp_f32_e32 v92, v92
	ds_read_b128 v[160:163], v201 offset:4096
	s_add_u32 s6, s15, 0x23a80000
	s_addc_u32 s7, s14, 0
	v_mfma_f32_16x16x32_bf16 v[0:3], v[164:167], v[216:219], v[0:3]
	v_cvt_pk_bf16_f32 v242, v80, v81
	v_mfma_f32_16x16x32_bf16 v[4:7], v[164:167], v[238:241], v[4:7]
	v_exp_f32_e32 v89, v89
	ds_read_b128 v[164:167], v209 offset:57344
	s_waitcnt vmcnt(4)
	ds_write_b128 v225, v[136:139] offset:32768
	s_waitcnt lgkmcnt(7)
	v_mfma_f32_16x16x32_bf16 v[68:71], v[168:171], v[116:119], v[68:71]
	v_exp_f32_e32 v93, v93
	v_mfma_f32_16x16x32_bf16 v[64:67], v[168:171], v[100:103], v[64:67]
	v_cvt_pk_bf16_f32 v243, v82, v83
	ds_read_b128 v[168:171], v202 offset:4096
	v_mfma_f32_16x16x32_bf16 v[12:15], v[172:175], v[238:241], v[12:15]
	v_exp_f32_e32 v90, v90
	v_mfma_f32_16x16x32_bf16 v[8:11], v[172:175], v[216:219], v[8:11]
	v_exp_f32_e32 v94, v94
	ds_read_b128 v[172:175], v209 offset:59392
	s_waitcnt lgkmcnt(7)
	v_mfma_f32_16x16x32_bf16 v[64:67], v[176:179], v[104:107], v[64:67]
	v_cvt_pk_bf16_f32 v204, v84, v85
	v_mfma_f32_16x16x32_bf16 v[68:71], v[176:179], v[120:123], v[68:71]
	v_exp_f32_e32 v91, v91
	ds_read_b128 v[176:179], v203 offset:4096
	ds_write_b128 v226, v[140:143] offset:32768
	v_mfma_f32_16x16x32_bf16 v[16:19], v[180:183], v[216:219], v[16:19]
	v_exp_f32_e32 v95, v95
	v_mfma_f32_16x16x32_bf16 v[20:23], v[180:183], v[238:241], v[20:23]
	v_cvt_pk_bf16_f32 v205, v86, v87
	v_add_f32_e32 v220, v220, v88
	ds_read_b128 v[180:183], v209 offset:61440
	s_waitcnt lgkmcnt(8)
	v_mfma_f32_16x16x32_bf16 v[68:71], v[230:233], v[124:127], v[68:71]
	v_add_f32_e32 v221, v221, v92
	v_add_f32_e32 v220, v220, v89
	v_mfma_f32_16x16x32_bf16 v[64:67], v[230:233], v[108:111], v[64:67]
	v_add_f32_e32 v221, v221, v93
	v_cvt_pk_bf16_f32 v244, v88, v89
	ds_read_b128 v[230:233], v246 offset:4096
	v_mfma_f32_16x16x32_bf16 v[28:31], v[234:237], v[238:241], v[28:31]
	v_cvt_pk_bf16_f32 v245, v90, v91
	v_cvt_pk_bf16_f32 v206, v92, v93
	v_mfma_f32_16x16x32_bf16 v[24:27], v[234:237], v[216:219], v[24:27]
	v_cvt_pk_bf16_f32 v207, v94, v95
	ds_read_b128 v[234:237], v209 offset:63488
	ds_write_b64 v227, v[148:149] offset:16384
	s_waitcnt lgkmcnt(9)
	v_mfma_f32_16x16x32_bf16 v[72:75], v[160:163], v[96:99], 0
	v_add_f32_e32 v220, v220, v90
	v_add_f32_e32 v221, v221, v94
	v_mfma_f32_16x16x32_bf16 v[76:79], v[160:163], v[112:115], 0
	v_add_f32_e32 v220, v220, v91
	v_add_f32_e32 v221, v221, v95
	ds_read_b128 v[160:163], v201 offset:8192
	v_mfma_f32_16x16x32_bf16 v[32:35], v[164:167], v[216:219], v[32:35]
	v_add_f32_e32 v194, v194, v220
	v_add_f32_e32 v195, v195, v221
	v_mfma_f32_16x16x32_bf16 v[36:39], v[164:167], v[238:241], v[36:39]
	v_exp_f32_e32 v64, v64
	ds_read_b128 v[164:167], v210 offset:49152
	s_waitcnt lgkmcnt(8)
	v_mfma_f32_16x16x32_bf16 v[76:79], v[168:171], v[116:119], v[76:79]
	v_exp_f32_e32 v68, v68
	v_mfma_f32_16x16x32_bf16 v[72:75], v[168:171], v[100:103], v[72:75]
	v_exp_f32_e32 v65, v65
	ds_read_b128 v[168:171], v202 offset:8192
	ds_write_b64 v228, v[150:151] offset:16384
	v_mfma_f32_16x16x32_bf16 v[44:47], v[172:175], v[238:241], v[44:47]
	v_exp_f32_e32 v69, v69
	v_mfma_f32_16x16x32_bf16 v[40:43], v[172:175], v[216:219], v[40:43]
	v_exp_f32_e32 v66, v66
	ds_read_b128 v[172:175], v210 offset:51200
	s_waitcnt lgkmcnt(8)
	v_mfma_f32_16x16x32_bf16 v[72:75], v[176:179], v[104:107], v[72:75]
	v_exp_f32_e32 v70, v70
	v_mfma_f32_16x16x32_bf16 v[76:79], v[176:179], v[120:123], v[76:79]
	v_exp_f32_e32 v67, v67
	ds_read_b128 v[176:179], v203 offset:8192
	v_mfma_f32_16x16x32_bf16 v[48:51], v[180:183], v[216:219], v[48:51]
	v_exp_f32_e32 v71, v71
	v_mfma_f32_16x16x32_bf16 v[52:55], v[180:183], v[238:241], v[52:55]
	v_add_f32_e32 v220, v64, v65
	ds_read_b128 v[180:183], v210 offset:53248
	ds_write_b64 v229, v[144:145] offset:16384
	s_waitcnt lgkmcnt(9)
	v_mfma_f32_16x16x32_bf16 v[76:79], v[230:233], v[124:127], v[76:79]
	v_add_f32_e32 v221, v68, v69
	v_mfma_f32_16x16x32_bf16 v[72:75], v[230:233], v[108:111], v[72:75]
	v_add_f32_e32 v220, v220, v66
	ds_read_b128 v[230:233], v246 offset:8192
	v_mfma_f32_16x16x32_bf16 v[60:63], v[234:237], v[238:241], v[60:63]
	v_add_f32_e32 v221, v221, v70
	v_add_f32_e32 v220, v220, v67
	v_mfma_f32_16x16x32_bf16 v[56:59], v[234:237], v[216:219], v[56:59]
	v_add_f32_e32 v221, v221, v71
	ds_read_b128 v[234:237], v210 offset:55296
	s_waitcnt lgkmcnt(8)
	v_mfma_f32_16x16x32_bf16 v[80:83], v[160:163], v[96:99], 0
	v_exp_f32_e32 v72, v72
	v_mfma_f32_16x16x32_bf16 v[84:87], v[160:163], v[112:115], 0
	v_exp_f32_e32 v76, v76
	ds_read_b128 v[160:163], v201 offset:12288
	ds_write_b64 v184, v[146:147] offset:16384
	v_mfma_f32_16x16x32_bf16 v[0:3], v[164:167], v[242:245], v[0:3]
	v_exp_f32_e32 v73, v73
	v_mfma_f32_16x16x32_bf16 v[4:7], v[164:167], v[204:207], v[4:7]
	v_exp_f32_e32 v77, v77
	ds_read_b128 v[164:167], v210 offset:57344
	s_waitcnt lgkmcnt(8)
	v_mfma_f32_16x16x32_bf16 v[84:87], v[168:171], v[116:119], v[84:87]
	v_exp_f32_e32 v74, v74
	v_mfma_f32_16x16x32_bf16 v[80:83], v[168:171], v[100:103], v[80:83]
	v_exp_f32_e32 v78, v78
	ds_read_b128 v[168:171], v202 offset:12288
	v_mfma_f32_16x16x32_bf16 v[12:15], v[172:175], v[204:207], v[12:15]
	v_exp_f32_e32 v75, v75
	v_mfma_f32_16x16x32_bf16 v[8:11], v[172:175], v[242:245], v[8:11]
	v_exp_f32_e32 v79, v79
	ds_read_b128 v[172:175], v210 offset:59392
	global_load_dwordx4 v[148:151], v198, s[8:9] offset:384
	s_waitcnt lgkmcnt(8)
	v_mfma_f32_16x16x32_bf16 v[80:83], v[176:179], v[104:107], v[80:83]
	v_add_f32_e32 v220, v220, v72
	v_add_f32_e32 v221, v221, v76
	v_mfma_f32_16x16x32_bf16 v[84:87], v[176:179], v[120:123], v[84:87]
	v_add_f32_e32 v220, v220, v73
	ds_read_b128 v[176:179], v203 offset:12288
	v_mfma_f32_16x16x32_bf16 v[16:19], v[180:183], v[242:245], v[16:19]
	v_add_f32_e32 v221, v221, v77
	v_add_f32_e32 v220, v220, v74
	v_mfma_f32_16x16x32_bf16 v[20:23], v[180:183], v[204:207], v[20:23]
	v_add_f32_e32 v221, v221, v78
	ds_read_b128 v[180:183], v210 offset:61440
	s_waitcnt lgkmcnt(7)
	v_mfma_f32_16x16x32_bf16 v[84:87], v[230:233], v[124:127], v[84:87]
	v_add_f32_e32 v220, v220, v75
	v_add_f32_e32 v221, v221, v79
	v_mfma_f32_16x16x32_bf16 v[80:83], v[230:233], v[108:111], v[80:83]
	v_cvt_pk_bf16_f32 v216, v64, v65
	ds_read_b128 v[230:233], v246 offset:12288
	global_load_dwordx4 v[144:147], v199, s[8:9] offset:384
	v_mfma_f32_16x16x32_bf16 v[28:31], v[234:237], v[204:207], v[28:31]
	v_cvt_pk_bf16_f32 v217, v66, v67
	v_cvt_pk_bf16_f32 v238, v68, v69
	v_mfma_f32_16x16x32_bf16 v[24:27], v[234:237], v[242:245], v[24:27]
	v_cvt_pk_bf16_f32 v239, v70, v71
	ds_read_b128 v[234:237], v210 offset:63488
	s_waitcnt lgkmcnt(6)
	v_mfma_f32_16x16x32_bf16 v[88:91], v[160:163], v[96:99], 0
	v_exp_f32_e32 v80, v80
	v_mfma_f32_16x16x32_bf16 v[92:95], v[160:163], v[112:115], 0
	v_exp_f32_e32 v84, v84
	v_mfma_f32_16x16x32_bf16 v[32:35], v[164:167], v[242:245], v[32:35]
	v_exp_f32_e32 v81, v81
	v_mfma_f32_16x16x32_bf16 v[36:39], v[164:167], v[204:207], v[36:39]
	v_exp_f32_e32 v85, v85
	global_load_dwordx4 v[136:139], v196, s[6:7]
	s_waitcnt lgkmcnt(5)
	v_mfma_f32_16x16x32_bf16 v[92:95], v[168:171], v[116:119], v[92:95]
	v_exp_f32_e32 v82, v82
	v_mfma_f32_16x16x32_bf16 v[88:91], v[168:171], v[100:103], v[88:91]
	v_exp_f32_e32 v86, v86
	s_waitcnt lgkmcnt(0)
	s_barrier
	ds_read_b128 v[160:163], v201 offset:16384
	ds_read_b128 v[164:167], v209 offset:0
	ds_read_b128 v[168:171], v202 offset:16384
	v_mfma_f32_16x16x32_bf16 v[44:47], v[172:175], v[204:207], v[44:47]
	v_exp_f32_e32 v83, v83
	v_mfma_f32_16x16x32_bf16 v[40:43], v[172:175], v[242:245], v[40:43]
	v_exp_f32_e32 v87, v87
	ds_read_b128 v[172:175], v209 offset:2048
	v_mfma_f32_16x16x32_bf16 v[88:91], v[176:179], v[104:107], v[88:91]
	v_add_f32_e32 v220, v220, v80
	v_add_f32_e32 v221, v221, v84
	v_mfma_f32_16x16x32_bf16 v[92:95], v[176:179], v[120:123], v[92:95]
	v_add_f32_e32 v220, v220, v81
	ds_read_b128 v[176:179], v203 offset:16384
	global_load_dwordx4 v[140:143], v197, s[6:7]
	v_mfma_f32_16x16x32_bf16 v[48:51], v[180:183], v[242:245], v[48:51]
	v_add_f32_e32 v221, v221, v85
	v_add_f32_e32 v220, v220, v82
	v_mfma_f32_16x16x32_bf16 v[52:55], v[180:183], v[204:207], v[52:55]
	v_add_f32_e32 v221, v221, v86
	ds_read_b128 v[180:183], v209 offset:4096
	v_mfma_f32_16x16x32_bf16 v[92:95], v[230:233], v[124:127], v[92:95]
	v_add_f32_e32 v220, v220, v83
	v_add_f32_e32 v221, v221, v87
	v_mfma_f32_16x16x32_bf16 v[88:91], v[230:233], v[108:111], v[88:91]
	v_cvt_pk_bf16_f32 v218, v72, v73
	ds_read_b128 v[230:233], v246 offset:16384
	s_add_u32 s8, s8, 0x200
	s_addc_u32 s9, s9, 0
	s_add_u32 s12, s12, 0x40000
	s_addc_u32 s13, s13, 0
	s_add_i32 s4, s4, 4
	s_cmp_lt_u32 s4, s101
	s_cselect_b64 vcc, -1, 0
	v_mfma_f32_16x16x32_bf16 v[60:63], v[234:237], v[204:207], v[60:63]
	v_cvt_pk_bf16_f32 v219, v74, v75
	v_cvt_pk_bf16_f32 v240, v76, v77
	v_mfma_f32_16x16x32_bf16 v[56:59], v[234:237], v[242:245], v[56:59]
	v_cvt_pk_bf16_f32 v241, v78, v79
	ds_read_b128 v[234:237], v209 offset:6144
	s_cbranch_vccnz .LBB0_734
	s_setprio 0
	s_waitcnt vmcnt(0)
	s_nop 7
	s_nop 7
	ds_swizzle_b32 v64, v194 offset:swizzle(SWAP,16)
	s_waitcnt lgkmcnt(0)
	v_add_f32_e32 v194, v194, v64
	v_mov_b32_e32 v65, v194
	s_nop 1
	v_permlane32_swap_b32_e32 v194, v65
	v_add_f32_e32 v194, v194, v65
	s_nop 0
	v_rcp_f32_e32 v66, v194
	ds_swizzle_b32 v64, v195 offset:swizzle(SWAP,16)
	s_waitcnt lgkmcnt(0)
	v_add_f32_e32 v195, v195, v64
	v_mov_b32_e32 v65, v195
	s_nop 1
	v_permlane32_swap_b32_e32 v195, v65
	v_add_f32_e32 v195, v195, v65
	s_nop 0
	v_rcp_f32_e32 v67, v195
	v_readlane_b32 s100, v250, 8
	v_mbcnt_lo_u32_b32 v68, -1, 0
	v_mbcnt_hi_u32_b32 v68, -1, v68
	v_and_b32_e32 v69, 15, v68
	v_lshrrev_b32_e32 v70, 4, v68
	s_lshr_b32 s101, s100, 1
	v_add_u32_e32 v69, s101, v69
	v_lshlrev_b32_e32 v69, 12, v69
	v_and_b32_e32 v71, 1, v70
	v_lshlrev_b32_e32 v71, 5, v71
	v_and_b32_e32 v70, 2, v70
	v_lshl_add_u32 v71, v70, 3, v71
	v_add_u32_e32 v70, v69, v71
	v_add_u32_e32 v71, 0x10000, v70
	v_mul_f32_e32 v0, v0, v66
	v_mul_f32_e32 v1, v1, v66
	v_mul_f32_e32 v2, v2, v66
	v_mul_f32_e32 v3, v3, v66
	v_mul_f32_e32 v8, v8, v66
	v_mul_f32_e32 v9, v9, v66
	v_mul_f32_e32 v10, v10, v66
	v_mul_f32_e32 v11, v11, v66
	v_cvt_pk_bf16_f32 v72, v0, v1
	v_cvt_pk_bf16_f32 v73, v2, v3
	v_cvt_pk_bf16_f32 v74, v8, v9
	v_cvt_pk_bf16_f32 v75, v10, v11
	s_nop 1
	v_permlane16_swap_b32_e32 v72, v74
	v_permlane16_swap_b32_e32 v73, v75
	s_nop 1
	global_store_dwordx4 v70, v[72:75], s[58:59] offset:0
	v_mul_f32_e32 v16, v16, v66
	v_mul_f32_e32 v17, v17, v66
	v_mul_f32_e32 v18, v18, v66
	v_mul_f32_e32 v19, v19, v66
	v_mul_f32_e32 v24, v24, v66
	v_mul_f32_e32 v25, v25, v66
	v_mul_f32_e32 v26, v26, v66
	v_mul_f32_e32 v27, v27, v66
	v_cvt_pk_bf16_f32 v76, v16, v17
	v_cvt_pk_bf16_f32 v77, v18, v19
	v_cvt_pk_bf16_f32 v78, v24, v25
	v_cvt_pk_bf16_f32 v79, v26, v27
	s_nop 1
	v_permlane16_swap_b32_e32 v76, v78
	v_permlane16_swap_b32_e32 v77, v79
	s_nop 1
	global_store_dwordx4 v70, v[76:79], s[58:59] offset:64
	v_mul_f32_e32 v32, v32, v66
	v_mul_f32_e32 v33, v33, v66
	v_mul_f32_e32 v34, v34, v66
	v_mul_f32_e32 v35, v35, v66
	v_mul_f32_e32 v40, v40, v66
	v_mul_f32_e32 v41, v41, v66
	v_mul_f32_e32 v42, v42, v66
	v_mul_f32_e32 v43, v43, v66
	v_cvt_pk_bf16_f32 v80, v32, v33
	v_cvt_pk_bf16_f32 v81, v34, v35
	v_cvt_pk_bf16_f32 v82, v40, v41
	v_cvt_pk_bf16_f32 v83, v42, v43
	s_nop 1
	v_permlane16_swap_b32_e32 v80, v82
	v_permlane16_swap_b32_e32 v81, v83
	s_nop 1
	global_store_dwordx4 v70, v[80:83], s[58:59] offset:128
	v_mul_f32_e32 v48, v48, v66
	v_mul_f32_e32 v49, v49, v66
	v_mul_f32_e32 v50, v50, v66
	v_mul_f32_e32 v51, v51, v66
	v_mul_f32_e32 v56, v56, v66
	v_mul_f32_e32 v57, v57, v66
	v_mul_f32_e32 v58, v58, v66
	v_mul_f32_e32 v59, v59, v66
	v_cvt_pk_bf16_f32 v84, v48, v49
	v_cvt_pk_bf16_f32 v85, v50, v51
	v_cvt_pk_bf16_f32 v86, v56, v57
	v_cvt_pk_bf16_f32 v87, v58, v59
	s_nop 1
	v_permlane16_swap_b32_e32 v84, v86
	v_permlane16_swap_b32_e32 v85, v87
	s_nop 1
	global_store_dwordx4 v70, v[84:87], s[58:59] offset:192
	v_mul_f32_e32 v4, v4, v67
	v_mul_f32_e32 v5, v5, v67
	v_mul_f32_e32 v6, v6, v67
	v_mul_f32_e32 v7, v7, v67
	v_mul_f32_e32 v12, v12, v67
	v_mul_f32_e32 v13, v13, v67
	v_mul_f32_e32 v14, v14, v67
	v_mul_f32_e32 v15, v15, v67
	v_cvt_pk_bf16_f32 v88, v4, v5
	v_cvt_pk_bf16_f32 v89, v6, v7
	v_cvt_pk_bf16_f32 v90, v12, v13
	v_cvt_pk_bf16_f32 v91, v14, v15
	s_nop 1
	v_permlane16_swap_b32_e32 v88, v90
	v_permlane16_swap_b32_e32 v89, v91
	s_nop 1
	global_store_dwordx4 v71, v[88:91], s[58:59] offset:0
	v_mul_f32_e32 v20, v20, v67
	v_mul_f32_e32 v21, v21, v67
	v_mul_f32_e32 v22, v22, v67
	v_mul_f32_e32 v23, v23, v67
	v_mul_f32_e32 v28, v28, v67
	v_mul_f32_e32 v29, v29, v67
	v_mul_f32_e32 v30, v30, v67
	v_mul_f32_e32 v31, v31, v67
	v_cvt_pk_bf16_f32 v92, v20, v21
	v_cvt_pk_bf16_f32 v93, v22, v23
	v_cvt_pk_bf16_f32 v94, v28, v29
	v_cvt_pk_bf16_f32 v95, v30, v31
	s_nop 1
	v_permlane16_swap_b32_e32 v92, v94
	v_permlane16_swap_b32_e32 v93, v95
	s_nop 1
	global_store_dwordx4 v71, v[92:95], s[58:59] offset:64
	v_mul_f32_e32 v36, v36, v67
	v_mul_f32_e32 v37, v37, v67
	v_mul_f32_e32 v38, v38, v67
	v_mul_f32_e32 v39, v39, v67
	v_mul_f32_e32 v44, v44, v67
	v_mul_f32_e32 v45, v45, v67
	v_mul_f32_e32 v46, v46, v67
	v_mul_f32_e32 v47, v47, v67
	v_cvt_pk_bf16_f32 v72, v36, v37
	v_cvt_pk_bf16_f32 v73, v38, v39
	v_cvt_pk_bf16_f32 v74, v44, v45
	v_cvt_pk_bf16_f32 v75, v46, v47
	s_nop 1
	v_permlane16_swap_b32_e32 v72, v74
	v_permlane16_swap_b32_e32 v73, v75
	s_nop 1
	global_store_dwordx4 v71, v[72:75], s[58:59] offset:128
	v_mul_f32_e32 v52, v52, v67
	v_mul_f32_e32 v53, v53, v67
	v_mul_f32_e32 v54, v54, v67
	v_mul_f32_e32 v55, v55, v67
	v_mul_f32_e32 v60, v60, v67
	v_mul_f32_e32 v61, v61, v67
	v_mul_f32_e32 v62, v62, v67
	v_mul_f32_e32 v63, v63, v67
	v_cvt_pk_bf16_f32 v76, v52, v53
	v_cvt_pk_bf16_f32 v77, v54, v55
	v_cvt_pk_bf16_f32 v78, v60, v61
	v_cvt_pk_bf16_f32 v79, v62, v63
	s_nop 1
	v_permlane16_swap_b32_e32 v76, v78
	v_permlane16_swap_b32_e32 v77, v79
	s_nop 1
	global_store_dwordx4 v71, v[76:79], s[58:59] offset:192
	s_barrier
